# baseline (speedup 1.0000x reference)
.LBB1_20:
	v_exp_f32_e32 v16, v16
	s_lshl_b32 s15, s13, 4
	v_exp_f32_e32 v17, v17
	s_add_i32 s15, s10, s15
	v_exp_f32_e32 v18, v18
	v_mov_b32_e32 v91, s15
	v_mov_b32_e32 v92, s14
	v_exp_f32_e32 v19, v19
	ds_write_b32 v91, v92
	v_exp_f32_e32 v20, v20
	v_exp_f32_e32 v21, v21
	v_exp_f32_e32 v22, v22
	v_exp_f32_e32 v23, v23
	v_exp_f32_e32 v24, v24
	v_exp_f32_e32 v25, v25
	v_exp_f32_e32 v26, v26
	v_exp_f32_e32 v27, v27
	v_exp_f32_e32 v28, v28
	v_exp_f32_e32 v29, v29
	v_exp_f32_e32 v30, v30
	v_exp_f32_e32 v31, v31
	v_exp_f32_e32 v32, v32
	v_exp_f32_e32 v33, v33
	v_exp_f32_e32 v34, v34
	v_exp_f32_e32 v35, v35
	v_exp_f32_e32 v36, v36
	v_exp_f32_e32 v37, v37
	v_exp_f32_e32 v38, v38
	v_exp_f32_e32 v39, v39
	v_exp_f32_e32 v40, v40
	v_exp_f32_e32 v41, v41
	v_exp_f32_e32 v42, v42
	v_exp_f32_e32 v43, v43
	v_exp_f32_e32 v44, v44
	v_exp_f32_e32 v45, v45
	v_exp_f32_e32 v46, v46
	v_exp_f32_e32 v47, v47
	v_lshl_add_u32 v91, s13, 14, v89
	v_pk_add_f32 v[92:93], v[16:17], v[18:19]
	v_pk_add_f32 v[94:95], v[20:21], v[22:23]
	v_pk_add_f32 v[92:93], v[92:93], v[24:25]
	v_pk_add_f32 v[94:95], v[94:95], v[26:27]
	v_pk_add_f32 v[92:93], v[92:93], v[28:29]
	v_pk_add_f32 v[94:95], v[94:95], v[30:31]
	v_cvt_pk_bf16_f32 v16, v16, v17
	v_cvt_pk_bf16_f32 v17, v18, v19
	v_cvt_pk_bf16_f32 v18, v20, v21
	v_cvt_pk_bf16_f32 v19, v22, v23
	ds_write_b128 v91, v[16:19]
	v_cvt_pk_bf16_f32 v16, v24, v25
	v_cvt_pk_bf16_f32 v17, v26, v27
	v_cvt_pk_bf16_f32 v18, v28, v29
	v_cvt_pk_bf16_f32 v19, v30, v31
	ds_write_b128 v91, v[16:19] offset:1024
	v_cvt_pk_bf16_f32 v16, v32, v33
	v_cvt_pk_bf16_f32 v17, v34, v35
	v_cvt_pk_bf16_f32 v18, v36, v37
	v_cvt_pk_bf16_f32 v19, v38, v39
	ds_write_b128 v91, v[16:19] offset:2048
	v_cvt_pk_bf16_f32 v16, v40, v41
	v_cvt_pk_bf16_f32 v17, v42, v43
	v_cvt_pk_bf16_f32 v18, v44, v45
	v_cvt_pk_bf16_f32 v19, v46, v47
	ds_write_b128 v91, v[16:19] offset:3072
	v_pk_add_f32 v[92:93], v[92:93], v[32:33]
	v_pk_add_f32 v[94:95], v[94:95], v[34:35]
	v_pk_add_f32 v[92:93], v[92:93], v[36:37]
	v_pk_add_f32 v[94:95], v[94:95], v[38:39]
	v_pk_add_f32 v[92:93], v[92:93], v[40:41]
	v_pk_add_f32 v[94:95], v[94:95], v[42:43]
	v_pk_add_f32 v[92:93], v[92:93], v[44:45]
	v_pk_add_f32 v[94:95], v[94:95], v[46:47]
	v_pk_add_f32 v[92:93], v[92:93], v[94:95]
	v_add_f32_e32 v94, v92, v93
	v_add_f32_e32 v99, v99, v94
	s_add_i32 s13, s5, 0x8000
	s_cmp_lg_u32 s5, 0x10000
	s_cselect_b32 s5, s13, 0
	s_add_i32 s11, s11, 1
	s_cmp_eq_u32 s11, 16
	s_waitcnt lgkmcnt(0)
	s_barrier
	s_cbranch_scc1 .LBB1_23
.LBB1_21:
	s_setprio 1
	v_add_u32_e32 v16, s5, v80
	ds_read_b128 v[32:35], v16
	ds_read_b128 v[36:39], v16 offset:256
	ds_read_b128 v[92:95], v16 offset:16384
	ds_read_b128 v[100:103], v16 offset:16640
	v_add_u32_e32 v16, s5, v81
	ds_read_b128 v[40:43], v16
	ds_read_b128 v[44:47], v16 offset:256
	ds_read_b128 v[104:107], v16 offset:16384
	ds_read_b128 v[108:111], v16 offset:16640
	s_waitcnt lgkmcnt(4)
	v_add_u32_e32 v91, s5, v82
	v_mfma_f32_32x32x16_bf16 v[16:31], v[32:35], v[128:131], v[0:15]
	ds_read_b128 v[32:35], v91
	v_mfma_f32_32x32x16_bf16 v[16:31], v[36:39], v[160:163], v[16:31]
	ds_read_b128 v[36:39], v91 offset:256
	ds_read_b128 v[112:115], v91 offset:16384
	ds_read_b128 v[116:119], v91 offset:16640
	s_waitcnt lgkmcnt(4)
	v_add_u32_e32 v91, s5, v83
	v_mfma_f32_32x32x16_bf16 v[16:31], v[40:43], v[132:135], v[16:31]
	ds_read_b128 v[40:43], v91
	v_mfma_f32_32x32x16_bf16 v[16:31], v[44:47], v[164:167], v[16:31]
	ds_read_b128 v[44:47], v91 offset:256
	ds_read_b128 v[120:123], v91 offset:16384
	ds_read_b128 v[124:127], v91 offset:16640
	s_waitcnt lgkmcnt(4)
	v_add_u32_e32 v91, s5, v84
	v_mfma_f32_32x32x16_bf16 v[16:31], v[32:35], v[136:139], v[16:31]
	ds_read_b128 v[32:35], v91
	v_mfma_f32_32x32x16_bf16 v[16:31], v[36:39], v[168:171], v[16:31]
	ds_read_b128 v[36:39], v91 offset:256
	ds_read_b128 v[194:197], v91 offset:16384
	ds_read_b128 v[198:201], v91 offset:16640
	s_waitcnt lgkmcnt(4)
	v_add_u32_e32 v91, s5, v85
	v_mfma_f32_32x32x16_bf16 v[16:31], v[40:43], v[140:143], v[16:31]
	ds_read_b128 v[40:43], v91
	v_mfma_f32_32x32x16_bf16 v[16:31], v[44:47], v[172:175], v[16:31]
	ds_read_b128 v[44:47], v91 offset:256
	ds_read_b128 v[202:205], v91 offset:16384
	ds_read_b128 v[206:209], v91 offset:16640
	s_waitcnt lgkmcnt(4)
	v_add_u32_e32 v91, s5, v86
	v_mfma_f32_32x32x16_bf16 v[16:31], v[32:35], v[144:147], v[16:31]
	ds_read_b128 v[32:35], v91
	v_mfma_f32_32x32x16_bf16 v[16:31], v[36:39], v[176:179], v[16:31]
	ds_read_b128 v[36:39], v91 offset:256
	ds_read_b128 v[210:213], v91 offset:16384
	ds_read_b128 v[214:217], v91 offset:16640
	s_waitcnt lgkmcnt(4)
	v_add_u32_e32 v91, s5, v87
	v_mfma_f32_32x32x16_bf16 v[16:31], v[40:43], v[148:151], v[16:31]
	ds_read_b128 v[40:43], v91
	v_mfma_f32_32x32x16_bf16 v[16:31], v[44:47], v[180:183], v[16:31]
	ds_read_b128 v[44:47], v91 offset:256
	ds_read_b128 v[218:221], v91 offset:16384
	ds_read_b128 v[222:225], v91 offset:16640
	s_waitcnt lgkmcnt(4)
	s_nop 0
	s_waitcnt lgkmcnt(0)
	v_mfma_f32_32x32x16_bf16 v[16:31], v[32:35], v[152:155], v[16:31]
	v_mfma_f32_32x32x16_bf16 v[16:31], v[36:39], v[184:187], v[16:31]
	v_mfma_f32_32x32x16_bf16 v[16:31], v[40:43], v[156:159], v[16:31]
	v_mfma_f32_32x32x16_bf16 v[16:31], v[44:47], v[188:191], v[16:31]
	s_setprio 0
	v_mfma_f32_32x32x16_bf16 v[32:47], v[92:95], v[128:131], v[0:15]
	s_and_b32 s13, s11, 1
	s_nop 8
	v_max_f32_e32 v91, v16, v17
	v_max3_f32 v91, v91, v18, v19
	v_max3_f32 v91, v91, v20, v21
	v_max3_f32 v91, v91, v22, v23
	v_max3_f32 v91, v91, v24, v25
	v_max3_f32 v91, v91, v26, v27
	v_mfma_f32_32x32x16_bf16 v[32:47], v[100:103], v[160:163], v[32:47]
	v_max3_f32 v91, v91, v28, v29
	v_max3_f32 v91, v91, v30, v31
	v_mfma_f32_32x32x16_bf16 v[32:47], v[104:107], v[132:135], v[32:47]
	v_mfma_f32_32x32x16_bf16 v[32:47], v[108:111], v[164:167], v[32:47]
	v_mfma_f32_32x32x16_bf16 v[32:47], v[112:115], v[136:139], v[32:47]
	v_mfma_f32_32x32x16_bf16 v[32:47], v[116:119], v[168:171], v[32:47]
	v_mfma_f32_32x32x16_bf16 v[32:47], v[120:123], v[140:143], v[32:47]
	v_mfma_f32_32x32x16_bf16 v[32:47], v[124:127], v[172:175], v[32:47]
	v_mfma_f32_32x32x16_bf16 v[32:47], v[194:197], v[144:147], v[32:47]
	v_mfma_f32_32x32x16_bf16 v[32:47], v[198:201], v[176:179], v[32:47]
	v_mfma_f32_32x32x16_bf16 v[32:47], v[202:205], v[148:151], v[32:47]
	v_mfma_f32_32x32x16_bf16 v[32:47], v[206:209], v[180:183], v[32:47]
	v_mfma_f32_32x32x16_bf16 v[32:47], v[210:213], v[152:155], v[32:47]
	v_mfma_f32_32x32x16_bf16 v[32:47], v[214:217], v[184:187], v[32:47]
	v_mfma_f32_32x32x16_bf16 v[32:47], v[218:221], v[156:159], v[32:47]
	v_mfma_f32_32x32x16_bf16 v[32:47], v[222:225], v[188:191], v[32:47]
	s_nop 11
	v_max3_f32 v92, v32, v33, v34
	v_max3_f32 v91, v91, v35, v36
	v_max3_f32 v92, v92, v37, v38
	v_max3_f32 v91, v91, v39, v40
	v_max3_f32 v92, v92, v41, v42
	v_max3_f32 v91, v91, v43, v44
	v_max3_f32 v92, v92, v45, v46
	v_max3_f32 v91, v91, v92, v47
	v_mov_b32_e32 v92, v91
	s_nop 1
	v_permlane32_swap_b32_e32 v91, v92
	v_max_f32_e32 v91, v91, v92
	v_cmp_ge_f32_e32 vcc, s12, v91
	s_cmp_eq_u64 vcc, exec
	s_cbranch_scc0 .LBB1_19
	s_mov_b32 s14, 0
	s_branch .LBB1_20
